# prologue silu loads de-serialized; MoE gather row-offset LIST loads issued together (one wait)
# speedup vs baseline: 1.0519x; 1.0114x over previous
; #define LAS __attribute__((address_space(3)))
; DI void phase_prologue(const Params& p, LAS unsigned char* lds, int G, int bid) {
;     ...
;         LAS float* s = (LAS float*)lds;
;         LAS float* part = (LAS float*)(lds + 40960);
;         for (int i = tid; i < 5 * DM; i += NTHREADS) { const int r = i / DM, k = i % DM; const float c = r < 4 ? p.in[1][r * DM + k] : p.in[3][k]; s[i] = c / (1.0f + __expf(-c)); }
;         __syncthreads();
.LBB0_7:
	s_load_dwordx16 s[52:67], s[0:1], 0x0
	s_load_dwordx16 s[4:19], s[0:1], 0x40
	s_cmp_gt_i32 s24, 0
	s_waitcnt lgkmcnt(0)
	v_writelane_b32 v251, s4, 16
	s_nop 1
	v_writelane_b32 v251, s5, 17
	v_writelane_b32 v251, s6, 18
	v_writelane_b32 v251, s7, 19
	v_writelane_b32 v251, s8, 20
	v_writelane_b32 v251, s9, 21
	v_writelane_b32 v251, s10, 22
	v_writelane_b32 v251, s11, 23
	v_writelane_b32 v251, s12, 24
	v_writelane_b32 v251, s13, 25
	v_writelane_b32 v251, s14, 26
	v_writelane_b32 v251, s15, 27
	v_writelane_b32 v251, s16, 28
	v_writelane_b32 v251, s17, 29
	v_writelane_b32 v251, s18, 30
	v_writelane_b32 v251, s19, 31
	s_load_dwordx16 s[4:19], s[0:1], 0x80
	s_cselect_b64 s[0:1], -1, 0
	s_cmp_lt_i32 s25, 1
	s_cselect_b64 s[2:3], -1, 0
	s_or_b64 s[0:1], s[0:1], s[2:3]
	s_waitcnt lgkmcnt(0)
	v_writelane_b32 v251, s4, 32
	s_and_b64 vcc, exec, s[0:1]
	s_nop 0
	v_writelane_b32 v251, s5, 33
	v_writelane_b32 v251, s6, 34
	v_writelane_b32 v251, s7, 35
	v_writelane_b32 v251, s8, 36
	v_writelane_b32 v251, s9, 37
	v_writelane_b32 v251, s10, 38
	v_writelane_b32 v251, s11, 39
	v_writelane_b32 v251, s12, 40
	v_writelane_b32 v251, s13, 41
	v_writelane_b32 v251, s14, 42
	v_writelane_b32 v251, s15, 43
	v_writelane_b32 v251, s16, 44
	v_writelane_b32 v251, s17, 45
	v_writelane_b32 v251, s18, 46
	v_writelane_b32 v251, s19, 47
	s_cbranch_vccnz .LBB0_157
	v_mov_b32_e32 v3, 0
	v_lshlrev_b32_e32 v66, 2, v0
	v_mov_b32_e32 v67, v3
	v_add_u32_e32 v1, 0, v66
	v_lshl_add_u64 v[4:5], s[54:55], 0, v[66:67]
	s_mov_b64 s[0:1], 0
	s_movk_i32 s4, 0x2000
	s_mov_b64 s[2:3], 0x800
	s_movk_i32 s5, 0x25ff
	v_mov_b32_e32 v6, v0
	v_add_u32_e32 v70, 0x0, v66
	v_add_u32_e32 v71, 0x1000, v66
	v_add_u32_e32 v72, 0x2000, v66
	v_add_u32_e32 v73, 0x3000, v66
	v_add_u32_e32 v74, 0x4000, v66
	v_add_u32_e32 v75, 0x5000, v66
	v_add_u32_e32 v76, 0x6000, v66
	v_add_u32_e32 v77, 0x7000, v66
	global_load_dword v100, v70, s[54:55] offset:0
	global_load_dword v101, v70, s[54:55] offset:2048
	global_load_dword v102, v71, s[54:55] offset:0
	global_load_dword v103, v71, s[54:55] offset:2048
	global_load_dword v104, v72, s[54:55] offset:0
	global_load_dword v105, v72, s[54:55] offset:2048
	global_load_dword v106, v73, s[54:55] offset:0
	global_load_dword v107, v73, s[54:55] offset:2048
	global_load_dword v108, v74, s[54:55] offset:0
	global_load_dword v109, v74, s[54:55] offset:2048
	global_load_dword v110, v75, s[54:55] offset:0
	global_load_dword v111, v75, s[54:55] offset:2048
	global_load_dword v112, v76, s[54:55] offset:0
	global_load_dword v113, v76, s[54:55] offset:2048
	global_load_dword v114, v77, s[54:55] offset:0
	global_load_dword v115, v77, s[54:55] offset:2048
	global_load_dword v116, v70, s[58:59] offset:0
	global_load_dword v117, v70, s[58:59] offset:2048
	global_load_dword v118, v71, s[58:59] offset:0
	global_load_dword v119, v71, s[58:59] offset:2048
	s_waitcnt vmcnt(19)
	v_mul_f32_e32 v7, 0xbfb8aa3b, v100
	v_exp_f32_e32 v7, v7
	s_nop 0
	v_add_f32_e32 v7, 1.0, v7
	v_div_scale_f32 v8, s[6:7], v7, v7, v100
	v_rcp_f32_e32 v9, v8
	v_div_scale_f32 v10, vcc, v100, v7, v100
	v_fma_f32 v11, -v8, v9, 1.0
	v_fmac_f32_e32 v9, v11, v9
	v_mul_f32_e32 v11, v10, v9
	v_fma_f32 v12, -v8, v11, v10
	v_fmac_f32_e32 v11, v12, v9
	v_fma_f32 v8, -v8, v11, v10
	v_div_fmas_f32 v8, v8, v9, v11
	v_div_fixup_f32 v2, v8, v7, v100
	ds_write_b32 v1, v2 offset:0
	s_waitcnt vmcnt(18)
	v_mul_f32_e32 v7, 0xbfb8aa3b, v101
	v_exp_f32_e32 v7, v7
	s_nop 0
	v_add_f32_e32 v7, 1.0, v7
	v_div_scale_f32 v8, s[6:7], v7, v7, v101
	v_rcp_f32_e32 v9, v8
	v_div_scale_f32 v10, vcc, v101, v7, v101
	v_fma_f32 v11, -v8, v9, 1.0
	v_fmac_f32_e32 v9, v11, v9
	v_mul_f32_e32 v11, v10, v9
	v_fma_f32 v12, -v8, v11, v10
	v_fmac_f32_e32 v11, v12, v9
	v_fma_f32 v8, -v8, v11, v10
	v_div_fmas_f32 v8, v8, v9, v11
	v_div_fixup_f32 v2, v8, v7, v101
	ds_write_b32 v1, v2 offset:2048
	s_waitcnt vmcnt(17)
	v_mul_f32_e32 v7, 0xbfb8aa3b, v102
	v_exp_f32_e32 v7, v7
	s_nop 0
	v_add_f32_e32 v7, 1.0, v7
	v_div_scale_f32 v8, s[6:7], v7, v7, v102
	v_rcp_f32_e32 v9, v8
	v_div_scale_f32 v10, vcc, v102, v7, v102
	v_fma_f32 v11, -v8, v9, 1.0
	v_fmac_f32_e32 v9, v11, v9
	v_mul_f32_e32 v11, v10, v9
	v_fma_f32 v12, -v8, v11, v10
	v_fmac_f32_e32 v11, v12, v9
	v_fma_f32 v8, -v8, v11, v10
	v_div_fmas_f32 v8, v8, v9, v11
	v_div_fixup_f32 v2, v8, v7, v102
	ds_write_b32 v1, v2 offset:4096
	s_waitcnt vmcnt(16)
	v_mul_f32_e32 v7, 0xbfb8aa3b, v103
	v_exp_f32_e32 v7, v7
	s_nop 0
	v_add_f32_e32 v7, 1.0, v7
	v_div_scale_f32 v8, s[6:7], v7, v7, v103
	v_rcp_f32_e32 v9, v8
	v_div_scale_f32 v10, vcc, v103, v7, v103
	v_fma_f32 v11, -v8, v9, 1.0
	v_fmac_f32_e32 v9, v11, v9
	v_mul_f32_e32 v11, v10, v9
	v_fma_f32 v12, -v8, v11, v10
	v_fmac_f32_e32 v11, v12, v9
	v_fma_f32 v8, -v8, v11, v10
	v_div_fmas_f32 v8, v8, v9, v11
	v_div_fixup_f32 v2, v8, v7, v103
	ds_write_b32 v1, v2 offset:6144
	s_waitcnt vmcnt(15)
	v_mul_f32_e32 v7, 0xbfb8aa3b, v104
	v_exp_f32_e32 v7, v7
	s_nop 0
	v_add_f32_e32 v7, 1.0, v7
	v_div_scale_f32 v8, s[6:7], v7, v7, v104
	v_rcp_f32_e32 v9, v8
	v_div_scale_f32 v10, vcc, v104, v7, v104
	v_fma_f32 v11, -v8, v9, 1.0
	v_fmac_f32_e32 v9, v11, v9
	v_mul_f32_e32 v11, v10, v9
	v_fma_f32 v12, -v8, v11, v10
	v_fmac_f32_e32 v11, v12, v9
	v_fma_f32 v8, -v8, v11, v10
	v_div_fmas_f32 v8, v8, v9, v11
	v_div_fixup_f32 v2, v8, v7, v104
	ds_write_b32 v1, v2 offset:8192
	s_waitcnt vmcnt(14)
	v_mul_f32_e32 v7, 0xbfb8aa3b, v105
	v_exp_f32_e32 v7, v7
	s_nop 0
	v_add_f32_e32 v7, 1.0, v7
	v_div_scale_f32 v8, s[6:7], v7, v7, v105
	v_rcp_f32_e32 v9, v8
	v_div_scale_f32 v10, vcc, v105, v7, v105
	v_fma_f32 v11, -v8, v9, 1.0
	v_fmac_f32_e32 v9, v11, v9
	v_mul_f32_e32 v11, v10, v9
	v_fma_f32 v12, -v8, v11, v10
	v_fmac_f32_e32 v11, v12, v9
	v_fma_f32 v8, -v8, v11, v10
	v_div_fmas_f32 v8, v8, v9, v11
	v_div_fixup_f32 v2, v8, v7, v105
	ds_write_b32 v1, v2 offset:10240
	s_waitcnt vmcnt(13)
; DI void phase_prologue(const Params& p, LAS unsigned char* lds, int G, int bid) {
;     ...
;         for (int i = tid; i < 5 * DM; i += NTHREADS) { const int r = i / DM, k = i % DM; const float c = r < 4 ? p.in[1][r * DM + k] : p.in[3][k]; s[i] = c / (1.0f + __expf(-c)); }
	v_mul_f32_e32 v7, 0xbfb8aa3b, v106
	v_exp_f32_e32 v7, v7
	s_nop 0
	v_add_f32_e32 v7, 1.0, v7
	v_div_scale_f32 v8, s[6:7], v7, v7, v106
	v_rcp_f32_e32 v9, v8
	v_div_scale_f32 v10, vcc, v106, v7, v106
	v_fma_f32 v11, -v8, v9, 1.0
	v_fmac_f32_e32 v9, v11, v9
	v_mul_f32_e32 v11, v10, v9
	v_fma_f32 v12, -v8, v11, v10
	v_fmac_f32_e32 v11, v12, v9
	v_fma_f32 v8, -v8, v11, v10
	v_div_fmas_f32 v8, v8, v9, v11
	v_div_fixup_f32 v2, v8, v7, v106
	ds_write_b32 v1, v2 offset:12288
	s_waitcnt vmcnt(12)
	v_mul_f32_e32 v7, 0xbfb8aa3b, v107
	v_exp_f32_e32 v7, v7
	s_nop 0
	v_add_f32_e32 v7, 1.0, v7
	v_div_scale_f32 v8, s[6:7], v7, v7, v107
	v_rcp_f32_e32 v9, v8
	v_div_scale_f32 v10, vcc, v107, v7, v107
	v_fma_f32 v11, -v8, v9, 1.0
	v_fmac_f32_e32 v9, v11, v9
	v_mul_f32_e32 v11, v10, v9
	v_fma_f32 v12, -v8, v11, v10
	v_fmac_f32_e32 v11, v12, v9
	v_fma_f32 v8, -v8, v11, v10
	v_div_fmas_f32 v8, v8, v9, v11
	v_div_fixup_f32 v2, v8, v7, v107
	ds_write_b32 v1, v2 offset:14336
	s_waitcnt vmcnt(11)
	v_mul_f32_e32 v7, 0xbfb8aa3b, v108
	v_exp_f32_e32 v7, v7
	s_nop 0
	v_add_f32_e32 v7, 1.0, v7
	v_div_scale_f32 v8, s[6:7], v7, v7, v108
	v_rcp_f32_e32 v9, v8
	v_div_scale_f32 v10, vcc, v108, v7, v108
	v_fma_f32 v11, -v8, v9, 1.0
	v_fmac_f32_e32 v9, v11, v9
	v_mul_f32_e32 v11, v10, v9
	v_fma_f32 v12, -v8, v11, v10
	v_fmac_f32_e32 v11, v12, v9
	v_fma_f32 v8, -v8, v11, v10
	v_div_fmas_f32 v8, v8, v9, v11
	v_div_fixup_f32 v2, v8, v7, v108
	ds_write_b32 v1, v2 offset:16384
	s_waitcnt vmcnt(10)
	v_mul_f32_e32 v7, 0xbfb8aa3b, v109
	v_exp_f32_e32 v7, v7
	s_nop 0
	v_add_f32_e32 v7, 1.0, v7
	v_div_scale_f32 v8, s[6:7], v7, v7, v109
	v_rcp_f32_e32 v9, v8
	v_div_scale_f32 v10, vcc, v109, v7, v109
	v_fma_f32 v11, -v8, v9, 1.0
	v_fmac_f32_e32 v9, v11, v9
	v_mul_f32_e32 v11, v10, v9
	v_fma_f32 v12, -v8, v11, v10
	v_fmac_f32_e32 v11, v12, v9
	v_fma_f32 v8, -v8, v11, v10
	v_div_fmas_f32 v8, v8, v9, v11
	v_div_fixup_f32 v2, v8, v7, v109
	ds_write_b32 v1, v2 offset:18432
	s_waitcnt vmcnt(9)
	v_mul_f32_e32 v7, 0xbfb8aa3b, v110
	v_exp_f32_e32 v7, v7
	s_nop 0
	v_add_f32_e32 v7, 1.0, v7
	v_div_scale_f32 v8, s[6:7], v7, v7, v110
	v_rcp_f32_e32 v9, v8
	v_div_scale_f32 v10, vcc, v110, v7, v110
	v_fma_f32 v11, -v8, v9, 1.0
	v_fmac_f32_e32 v9, v11, v9
	v_mul_f32_e32 v11, v10, v9
	v_fma_f32 v12, -v8, v11, v10
	v_fmac_f32_e32 v11, v12, v9
	v_fma_f32 v8, -v8, v11, v10
	v_div_fmas_f32 v8, v8, v9, v11
	v_div_fixup_f32 v2, v8, v7, v110
	ds_write_b32 v1, v2 offset:20480
	s_waitcnt vmcnt(8)
	v_mul_f32_e32 v7, 0xbfb8aa3b, v111
	v_exp_f32_e32 v7, v7
	s_nop 0
	v_add_f32_e32 v7, 1.0, v7
	v_div_scale_f32 v8, s[6:7], v7, v7, v111
	v_rcp_f32_e32 v9, v8
	v_div_scale_f32 v10, vcc, v111, v7, v111
	v_fma_f32 v11, -v8, v9, 1.0
	v_fmac_f32_e32 v9, v11, v9
	v_mul_f32_e32 v11, v10, v9
	v_fma_f32 v12, -v8, v11, v10
	v_fmac_f32_e32 v11, v12, v9
	v_fma_f32 v8, -v8, v11, v10
	v_div_fmas_f32 v8, v8, v9, v11
	v_div_fixup_f32 v2, v8, v7, v111
	ds_write_b32 v1, v2 offset:22528
	s_waitcnt vmcnt(7)
	v_mul_f32_e32 v7, 0xbfb8aa3b, v112
	v_exp_f32_e32 v7, v7
	s_nop 0
	v_add_f32_e32 v7, 1.0, v7
	v_div_scale_f32 v8, s[6:7], v7, v7, v112
	v_rcp_f32_e32 v9, v8
	v_div_scale_f32 v10, vcc, v112, v7, v112
	v_fma_f32 v11, -v8, v9, 1.0
	v_fmac_f32_e32 v9, v11, v9
	v_mul_f32_e32 v11, v10, v9
	v_fma_f32 v12, -v8, v11, v10
	v_fmac_f32_e32 v11, v12, v9
	v_fma_f32 v8, -v8, v11, v10
	v_div_fmas_f32 v8, v8, v9, v11
	v_div_fixup_f32 v2, v8, v7, v112
	ds_write_b32 v1, v2 offset:24576
	s_waitcnt vmcnt(6)
	v_mul_f32_e32 v7, 0xbfb8aa3b, v113
	v_exp_f32_e32 v7, v7
	s_nop 0
	v_add_f32_e32 v7, 1.0, v7
	v_div_scale_f32 v8, s[6:7], v7, v7, v113
	v_rcp_f32_e32 v9, v8
	v_div_scale_f32 v10, vcc, v113, v7, v113
	v_fma_f32 v11, -v8, v9, 1.0
	v_fmac_f32_e32 v9, v11, v9
	v_mul_f32_e32 v11, v10, v9
	v_fma_f32 v12, -v8, v11, v10
	v_fmac_f32_e32 v11, v12, v9
	v_fma_f32 v8, -v8, v11, v10
	v_div_fmas_f32 v8, v8, v9, v11
	v_div_fixup_f32 v2, v8, v7, v113
	ds_write_b32 v1, v2 offset:26624
	s_waitcnt vmcnt(5)
;     DI NoBias bias(int) const { return NoBias(); }
;     DI WinBias bias(int q) const { const int j = tid_(q); WinBias B; B.base = j < 4 ? 100 : qpos - (k0base + 64 * (j - 4)) + 128; return B; }
; DI void phase_prologue(const Params& p, LAS unsigned char* lds, int G, int bid) {
;     ...
;         for (int i = tid; i < 5 * DM; i += NTHREADS) { const int r = i / DM, k = i % DM; const float c = r < 4 ? p.in[1][r * DM + k] : p.in[3][k]; s[i] = c / (1.0f + __expf(-c)); }
;         __syncthreads();
;         float* MOD = (float*)(ws + WS_MOD);
;         for (int chunk = bid; chunk < 256; chunk += G) {
;             const int layer = chunk >> 7, n0 = (chunk & 127) * 96;
;             const float* W = layer ? p.in[27] : p.in[7]; const float* bias = layer ? p.in[28] : p.in[8];
;             const int cg = tid % 24, ks = tid / 24;
;             if (ks < 16) {
;                 f32x4 acc[5];
; #pragma unroll
;                 for (int r = 0; r < 5; ++r) acc[r] = (f32x4){0.f, 0.f, 0.f, 0.f};
;                 const float* wp = W + (size_t)(ks * 128) * MODN + n0 + 4 * cg;
	v_mul_f32_e32 v7, 0xbfb8aa3b, v114
	v_exp_f32_e32 v7, v7
	s_nop 0
	v_add_f32_e32 v7, 1.0, v7
	v_div_scale_f32 v8, s[6:7], v7, v7, v114
	v_rcp_f32_e32 v9, v8
	v_div_scale_f32 v10, vcc, v114, v7, v114
	v_fma_f32 v11, -v8, v9, 1.0
	v_fmac_f32_e32 v9, v11, v9
	v_mul_f32_e32 v11, v10, v9
	v_fma_f32 v12, -v8, v11, v10
	v_fmac_f32_e32 v11, v12, v9
	v_fma_f32 v8, -v8, v11, v10
	v_div_fmas_f32 v8, v8, v9, v11
	v_div_fixup_f32 v2, v8, v7, v114
	ds_write_b32 v1, v2 offset:28672
	s_waitcnt vmcnt(4)
	v_mul_f32_e32 v7, 0xbfb8aa3b, v115
	v_exp_f32_e32 v7, v7
	s_nop 0
	v_add_f32_e32 v7, 1.0, v7
	v_div_scale_f32 v8, s[6:7], v7, v7, v115
	v_rcp_f32_e32 v9, v8
	v_div_scale_f32 v10, vcc, v115, v7, v115
	v_fma_f32 v11, -v8, v9, 1.0
	v_fmac_f32_e32 v9, v11, v9
	v_mul_f32_e32 v11, v10, v9
	v_fma_f32 v12, -v8, v11, v10
	v_fmac_f32_e32 v11, v12, v9
	v_fma_f32 v8, -v8, v11, v10
	v_div_fmas_f32 v8, v8, v9, v11
	v_div_fixup_f32 v2, v8, v7, v115
	ds_write_b32 v1, v2 offset:30720
	s_waitcnt vmcnt(3)
	v_mul_f32_e32 v7, 0xbfb8aa3b, v116
	v_exp_f32_e32 v7, v7
	s_nop 0
	v_add_f32_e32 v7, 1.0, v7
	v_div_scale_f32 v8, s[6:7], v7, v7, v116
	v_rcp_f32_e32 v9, v8
	v_div_scale_f32 v10, vcc, v116, v7, v116
	v_fma_f32 v11, -v8, v9, 1.0
	v_fmac_f32_e32 v9, v11, v9
	v_mul_f32_e32 v11, v10, v9
	v_fma_f32 v12, -v8, v11, v10
	v_fmac_f32_e32 v11, v12, v9
	v_fma_f32 v8, -v8, v11, v10
	v_div_fmas_f32 v8, v8, v9, v11
	v_div_fixup_f32 v2, v8, v7, v116
	ds_write_b32 v1, v2 offset:32768
	s_waitcnt vmcnt(2)
	v_mul_f32_e32 v7, 0xbfb8aa3b, v117
	v_exp_f32_e32 v7, v7
	s_nop 0
	v_add_f32_e32 v7, 1.0, v7
	v_div_scale_f32 v8, s[6:7], v7, v7, v117
	v_rcp_f32_e32 v9, v8
	v_div_scale_f32 v10, vcc, v117, v7, v117
	v_fma_f32 v11, -v8, v9, 1.0
	v_fmac_f32_e32 v9, v11, v9
	v_mul_f32_e32 v11, v10, v9
	v_fma_f32 v12, -v8, v11, v10
	v_fmac_f32_e32 v11, v12, v9
	v_fma_f32 v8, -v8, v11, v10
	v_div_fmas_f32 v8, v8, v9, v11
	v_div_fixup_f32 v2, v8, v7, v117
	ds_write_b32 v1, v2 offset:34816
	s_waitcnt vmcnt(1)
	v_mul_f32_e32 v7, 0xbfb8aa3b, v118
	v_exp_f32_e32 v7, v7
	s_nop 0
	v_add_f32_e32 v7, 1.0, v7
	v_div_scale_f32 v8, s[6:7], v7, v7, v118
	v_rcp_f32_e32 v9, v8
	v_div_scale_f32 v10, vcc, v118, v7, v118
	v_fma_f32 v11, -v8, v9, 1.0
	v_fmac_f32_e32 v9, v11, v9
	v_mul_f32_e32 v11, v10, v9
	v_fma_f32 v12, -v8, v11, v10
	v_fmac_f32_e32 v11, v12, v9
	v_fma_f32 v8, -v8, v11, v10
	v_div_fmas_f32 v8, v8, v9, v11
	v_div_fixup_f32 v2, v8, v7, v118
	ds_write_b32 v1, v2 offset:36864
	s_waitcnt vmcnt(0)
	v_mul_f32_e32 v7, 0xbfb8aa3b, v119
	v_exp_f32_e32 v7, v7
	s_nop 0
	v_add_f32_e32 v7, 1.0, v7
	v_div_scale_f32 v8, s[6:7], v7, v7, v119
	v_rcp_f32_e32 v9, v8
	v_div_scale_f32 v10, vcc, v119, v7, v119
	v_fma_f32 v11, -v8, v9, 1.0
	v_fmac_f32_e32 v9, v11, v9
	v_mul_f32_e32 v11, v10, v9
	v_fma_f32 v12, -v8, v11, v10
	v_fmac_f32_e32 v11, v12, v9
	v_fma_f32 v8, -v8, v11, v10
	v_div_fmas_f32 v8, v8, v9, v11
	v_div_fixup_f32 v2, v8, v7, v119
	ds_write_b32 v1, v2 offset:38912
	s_or_b64 exec, exec, s[0:1]
	v_and_b32_e32 v1, 31, v0
	v_and_b32_e32 v2, 15, v0
	v_cvt_f32_ubyte0_e32 v67, v1
	v_cvt_f32_ubyte0_e32 v1, v2
	v_mul_f32_e32 v3, 0xbed49a78, v67
	v_mul_f32_e32 v2, 0xbf549a78, v1
	s_mov_b32 s0, 0xc2fc0000
	s_cmpk_gt_i32 s22, 0xff
	v_cmp_gt_f32_e32 vcc, s0, v3
	s_mov_b32 s9, 0
	v_cmp_gt_f32_e64 s[2:3], s0, v2
	s_waitcnt lgkmcnt(0)
	s_barrier
	s_cbranch_scc1 .LBB0_19
	v_mul_u32_u24_e32 v2, 0xaab, v0
	s_movk_i32 s0, 0x2ab
	v_lshrrev_b32_e32 v3, 16, v2
	v_mul_u32_u24_sdwa v5, v0, s0 dst_sel:DWORD dst_unused:UNUSED_PAD src0_sel:WORD_0 src1_sel:DWORD
	v_mul_lo_u16_e32 v2, 24, v3
	v_lshrrev_b32_e32 v68, 16, v5
	v_sub_u16_e32 v2, v0, v2
	v_mul_lo_u16_e32 v5, 0x60, v68
	v_sub_u16_e32 v70, v0, v5
	v_lshlrev_b16_e32 v2, 2, v2
	v_mul_u32_u24_e32 v4, 0x180000, v3
	s_movk_i32 s0, 0x180
	v_lshl_add_u32 v69, v3, 9, 0
	v_mov_b32_e32 v73, 0
	v_lshlrev_b32_e32 v2, 2, v2
	v_lshlrev_b32_e32 v6, 2, v70
	v_mul_u32_u24_e32 v7, 0x780, v3
	v_mul_lo_u16_e32 v3, 0x180, v68
	v_cmp_gt_u32_e64 s[4:5], s0, v0
	s_movk_i32 s0, 0x1e0
	s_add_u32 s10, s50, 0x10000
	v_add_u32_e32 v5, 0, v2
	v_add3_u32 v71, 0, v6, v3
	v_lshlrev_b32_e32 v72, 2, v4
	v_mov_b32_e32 v3, v73
	v_cmp_gt_u32_e64 s[6:7], s0, v0
	s_addc_u32 s11, s51, 0
	v_add_u32_e32 v78, 0xa000, v71
	v_lshl_add_u64 v[74:75], v[72:73], 0, v[2:3]
	s_mov_b32 s16, 0xc000
	v_add_u32_e32 v79, v5, v7
	v_lshlrev_b32_e32 v72, 2, v70
	v_mov_b32_e32 v80, 0x180
	s_mov_b32 s17, s22
	s_mov_b32 s18, s22
	s_branch .LBB0_13

; #define PG8_STAGE_A(bufoff, gbase, h, VG) do { if constexpr (Sched::GATHER) { PG8_STAGE(bufoff, gbase, VG[h]); } else { PG8_STAGE(bufoff, (gbase) + (h) * ahs, voffA); } } while (0)
; #define PG8_STAGE_B(bufoff, gbase, h) PG8_STAGE(bufoff, (gbase) + (h) * bhs, voffB)
; #define PG8_WAIT_V(n) asm volatile("s_waitcnt vmcnt(" #n ")" ::: "memory")
; #define PG8_BAR __builtin_amdgcn_s_barrier()
;     DI unsigned rowoff(const pg8::GU& u, int r) const { const int gr = 256 * u.pm + r; const int tok = gr < MT[128 + u.e] ? LIST[(size_t)u.e * MOE_CAP + gr] : NTOK; return (unsigned)tok * (unsigned)lda; }
;     DI bool next(int i, pg8::GU& u) const { int pm, pn; if (!T.tile(i, pm, pn)) return false; u.pm = pm; u.pn = pn; u.e = 0; u.aux = 0; u.h1 = 0; u.a = A + (size_t)pm * 256 * lda; u.b = Bt + (size_t)pn * 256 * ldb; return true; }
; template <class Epi, class Sched>
; DI void gemm_phase(LAS unsigned char* lds, const Sched& S, const Epi& E) {
;     ...
;     if constexpr (Sched::GATHER) {
; #pragma unroll
;         for (int h = 0; h < 2; ++h)
; #pragma unroll
;             for (int i = 0; i < 2; ++i) { vc[h][i] = S.rowoff(cur, RR[i] + 128 * h) + (unsigned)(CC[i] * 2); vn[h][i] = vc[h][i]; }
;     } else {
; #pragma unroll
;         for (int h = 0; h < 2; ++h)
; #pragma unroll
;             for (int i = 0; i < 2; ++i) { vc[h][i] = 0u; vn[h][i] = 0u; }
;     }
;     const char* cA = cur.a; const char* cB = cur.b;
;     if constexpr (PG8_SP2) {
;         PG8_STAGE_B(PG8_SB(0, 0), cB, 0); PG8_STAGE_B(PG8_SB(0, 1), cB, 1); PG8_STAGE_A(PG8_SA(0, 0), cA, 0, vc); PG8_STAGE_A(PG8_SA(0, 1), cA, 1, vc);
;         if (wr == 1) PG8_BAR;
;         PG8_WAIT_V(2); PG8_BAR;
;         PG8_STAGE_B(PG8_SB(1, 0), cB + kstep, 0); PG8_STAGE_A(PG8_SA(1, 0), cA + kstep, 0, vc); PG8_STAGE_B(PG8_SB(1, 1), cB + kstep, 1);
;         PG8_WAIT_V(6); PG8_BAR;
;     DI bool next(int i, pg8::GU& u) const {
;         const int L = i * G + c, T = MT[64 + 32]; if (L >= T * 4) return false;
;         const int rt = L >> 2, ct = L & 3; const int e = MT[192 + rt];
;         const int lt = rt - MT[64 + e];
;         u.e = e; u.pm = lt; u.pn = ct; u.aux = MT[e] + 256 * lt; u.h1 = (MT[128 + e] - 256 * lt) <= 128; u.a = Hb; u.b = EG + (size_t)e * estride + (size_t)ct * 128 * ldb; return true;
;     }
.LBB0_870:
.LBB0_871:
	v_and_b32_e32 v198, 32, v2
	v_or_b32_e32 v223, 31, v2
	v_lshrrev_b32_e32 v1, 1, v0
	s_andn2_b64 vcc, exec, s[6:7]
	v_lshlrev_b32_e32 v199, 2, v0
	s_cbranch_vccnz .LBB0_915
	v_bfe_u32 v11, v0, 2, 4
	v_and_or_b32 v200, v2, 48, v11
	v_lshlrev_b32_e32 v2, 2, v3
	v_add_u32_e32 v2, 0, v2
	v_add_u32_e32 v2, 0x22240, v2
	ds_read_b32 v9, v2
	s_add_u32 s10, s50, 0x32c0e000
	s_mov_b32 s3, 0x9000
	s_addc_u32 s11, s51, 0
	v_mul_hi_i32 v5, v3, s3
	v_mul_lo_u32 v4, v3, s3
	v_lshl_add_u64 v[2:3], s[10:11], 0, v[4:5]
	v_or_b32_e32 v4, s2, v200
	s_waitcnt lgkmcnt(0)
	v_cmp_lt_i32_e32 vcc, v4, v9
	v_mov_b32_e32 v8, 0x2400
	v_mov_b32_e32 v7, 0x2400
	s_and_saveexec_b64 s[6:7], vcc
	s_cbranch_execz .LBB0_874
	v_ashrrev_i32_e32 v5, 31, v4
	v_lshl_add_u64 v[4:5], v[4:5], 2, v[2:3]
	global_load_dword v7, v[4:5], off
.LBB0_874:
	s_or_b64 exec, exec, s[6:7]
	v_bfe_u32 v4, v0, 3, 25
	v_or_b32_e32 v6, 64, v4
	s_movk_i32 s3, 0x70
	v_and_or_b32 v224, v6, s3, v11
	v_or_b32_e32 v4, s2, v224
	v_cmp_lt_i32_e32 vcc, v4, v9
	s_and_saveexec_b64 s[6:7], vcc
	s_cbranch_execz .LBB0_876
	v_ashrrev_i32_e32 v5, 31, v4
	v_lshl_add_u64 v[4:5], v[4:5], 2, v[2:3]
	global_load_dword v8, v[4:5], off
.LBB0_876:
	s_or_b64 exec, exec, s[6:7]
	s_or_b32 s9, s2, 0x80
	v_or_b32_e32 v4, s9, v200
	v_cmp_lt_i32_e32 vcc, v4, v9
	v_mov_b32_e32 v5, 0x2400
	v_mov_b32_e32 v11, 0x2400
	s_and_saveexec_b64 s[6:7], vcc
	s_cbranch_execz .LBB0_878
	v_mov_b32_e32 v201, 0
	s_ashr_i32 s3, s2, 31
	v_lshl_add_u64 v[12:13], s[2:3], 0, v[200:201]
	v_lshl_add_u64 v[12:13], v[12:13], 2, v[2:3]
	global_load_dword v11, v[12:13], off offset:512
.LBB0_878:
	s_or_b64 exec, exec, s[6:7]
	v_add_u32_e32 v4, s9, v224
	v_lshrrev_b32_e32 v12, 2, v0
	v_lshlrev_b32_e32 v13, 4, v0
	v_cmp_lt_i32_e32 vcc, v4, v9
	s_and_saveexec_b64 s[2:3], vcc
	s_cbranch_execz .LBB0_880
	v_ashrrev_i32_e32 v5, 31, v4
	v_lshl_add_u64 v[2:3], v[4:5], 2, v[2:3]
	global_load_dword v5, v[2:3], off
.LBB0_880:
	s_or_b64 exec, exec, s[2:3]
	s_waitcnt vmcnt(0)
	v_lshlrev_b32_e32 v7, 11, v7
	v_lshlrev_b32_e32 v8, 11, v8
	v_lshlrev_b32_e32 v11, 11, v11
	v_lshlrev_b32_e32 v5, 11, v5
	v_and_b32_e32 v2, 32, v0
	v_bitop3_b32 v2, v13, v2, 48 bitop3:0x6c
	v_and_or_b32 v225, v0, 64, v2
	s_lshr_b32 s3, s8, 6
	v_lshlrev_b32_e32 v2, 1, v12
	v_lshrrev_b32_e32 v3, 5, v0
	s_lshl_b32 s6, s3, 10
	v_and_b32_e32 v2, 24, v2
	v_and_b32_e32 v3, 4, v3
	v_and_b32_e32 v4, 3, v12
	v_or3_b32 v2, v3, v4, v2
	s_add_i32 s69, s6, 0
	s_lshr_b32 s2, s8, 8
	v_or_b32_e32 v3, v2, v198
	s_movk_i32 s7, 0x60
	s_add_i32 s70, s69, 0x10000
	s_add_i32 s71, s69, 0x12000
	v_lshl_or_b32 v202, v3, 11, v225
	v_and_or_b32 v2, v6, s7, v2
	s_mov_b32 m0, s70
	s_add_u32 s6, s4, 0x8000000
	v_lshl_or_b32 v204, v2, 11, v225
	global_load_lds_dwordx4 v202, s[4:5]
	s_mov_b32 m0, s71
	s_addc_u32 s7, s5, 0
	s_add_i32 s72, s69, 0x14000
	global_load_lds_dwordx4 v204, s[4:5]
	s_mov_b32 m0, s72
	s_add_i32 s73, s69, 0x16000
	global_load_lds_dwordx4 v202, s[6:7]
	s_mov_b32 m0, s73
	v_or_b32_e32 v210, v7, v225
	global_load_lds_dwordx4 v204, s[6:7]
	s_mov_b32 m0, s69
	s_add_i32 s74, s69, 0x2000
	v_or_b32_e32 v208, v8, v225
	global_load_lds_dwordx4 v210, s[40:41]
	s_mov_b32 m0, s74
	s_add_i32 s75, s69, 0x4000
	v_or_b32_e32 v206, v11, v225
	global_load_lds_dwordx4 v208, s[40:41]
	s_mov_b32 m0, s75
	s_add_i32 s76, s69, 0x6000
	v_or_b32_e32 v212, v5, v225
	global_load_lds_dwordx4 v206, s[40:41]
	s_mov_b32 m0, s76
	v_mov_b32_e32 v67, 0
	global_load_lds_dwordx4 v212, s[40:41]
	v_mov_b32_e32 v203, v67
	v_mov_b32_e32 v205, v67
	v_mov_b32_e32 v211, v67
	v_mov_b32_e32 v209, v67
	s_cmp_eq_u32 s2, 1
	s_mov_b32 s77, 0
	v_lshl_add_u64 v[8:9], s[4:5], 0, v[202:203]
	v_lshl_add_u64 v[4:5], s[4:5], 0, v[204:205]
	v_lshl_add_u64 v[6:7], s[40:41], 0, v[210:211]
	v_lshl_add_u64 v[2:3], s[40:41], 0, v[208:209]
	s_cselect_b64 s[12:13], -1, 0
	s_cmp_lg_u32 s2, 1
	s_movk_i32 s78, 0x4000
	s_cbranch_scc1 .LBB0_882
	s_barrier

;     DI unsigned rowoff(const pg8::GU& u, int r) const { const int gr = 256 * u.pm + r; const int tok = gr < MT[128 + u.e] ? LIST[(size_t)u.e * MOE_CAP + gr] : NTOK; return (unsigned)tok * (unsigned)lda; }
;     DI bool next(int i, pg8::GU& u) const { int pm, pn; if (!T.tile(i, pm, pn)) return false; u.pm = pm; u.pn = pn; u.e = 0; u.aux = 0; u.h1 = 0; u.a = A + (size_t)pm * 256 * lda; u.b = Bt + (size_t)pn * 256 * ldb; return true; }
; template <class Epi, class Sched>
; DI void gemm_phase(LAS unsigned char* lds, const Sched& S, const Epi& E) {
;     ...
;         if constexpr (Sched::GATHER) {
;             if (has_next) {
; #pragma unroll
;                 for (int h = 0; h < 2; ++h)
; #pragma unroll
;                     for (int i = 0; i < 2; ++i) vn[h][i] = S.rowoff(nxt, RR[i] + 128 * h) + (unsigned)(CC[i] * 2);
;     DI bool next(int i, pg8::GU& u) const {
;         const int L = i * G + c, T = MT[64 + 32]; if (L >= T * 4) return false;
;         const int rt = L >> 2, ct = L & 3; const int e = MT[192 + rt];
;         const int lt = rt - MT[64 + e];
;         u.e = e; u.pm = lt; u.pn = ct; u.aux = MT[e] + 256 * lt; u.h1 = (MT[128 + e] - 256 * lt) <= 128; u.a = Hb; u.b = EG + (size_t)e * estride + (size_t)ct * 128 * ldb; return true;
;     }
.LBB0_887:
	v_cndmask_b32_e64 v2, 0, 1, s[6:7]
	v_cmp_ne_u32_e64 s[2:3], 1, v2
	s_andn2_b64 vcc, exec, s[6:7]
	v_mov_b32_e32 v238, v212
	v_mov_b32_e32 v235, v206
	v_mov_b32_e32 v236, v208
	v_mov_b32_e32 v237, v210
	s_cbranch_vccnz .LBB0_897
	v_lshlrev_b32_e32 v2, 2, v232
	v_add_u32_e32 v2, 0, v2
	v_add_u32_e32 v2, 0x22240, v2
	ds_read_b32 v8, v2
	s_lshl_b32 s6, s92, 8
	v_mul_hi_i32 v3, v232, s87
	v_mul_lo_u32 v2, v232, s87
	v_or_b32_e32 v4, s6, v200
	v_lshl_add_u64 v[2:3], s[10:11], 0, v[2:3]
	s_waitcnt lgkmcnt(0)
	v_cmp_lt_i32_e32 vcc, v4, v8
	v_mov_b32_e32 v7, 0x2400
	v_mov_b32_e32 v6, 0x2400
	s_and_saveexec_b64 s[8:9], vcc
	s_cbranch_execz .LBB0_890
	v_ashrrev_i32_e32 v5, 31, v4
	v_lshl_add_u64 v[4:5], v[4:5], 2, v[2:3]
	global_load_dword v6, v[4:5], off
.LBB0_890:
	s_or_b64 exec, exec, s[8:9]
	v_or_b32_e32 v4, s6, v224
	v_cmp_lt_i32_e32 vcc, v4, v8
	s_and_saveexec_b64 s[8:9], vcc
	s_cbranch_execz .LBB0_892
	v_ashrrev_i32_e32 v5, 31, v4
	v_lshl_add_u64 v[4:5], v[4:5], 2, v[2:3]
	global_load_dword v7, v[4:5], off
.LBB0_892:
	s_or_b64 exec, exec, s[8:9]
	s_or_b32 s54, s6, 0x80
	v_or_b32_e32 v4, s54, v200
	v_cmp_lt_i32_e32 vcc, v4, v8
	v_mov_b32_e32 v5, 0x2400
	v_mov_b32_e32 v9, 0x2400
	s_and_saveexec_b64 s[8:9], vcc
	s_cbranch_execz .LBB0_894
	s_ashr_i32 s7, s6, 31
	v_lshl_add_u64 v[12:13], s[6:7], 0, v[200:201]
	v_lshl_add_u64 v[12:13], v[12:13], 2, v[2:3]
	global_load_dword v9, v[12:13], off offset:512
.LBB0_894:
	s_or_b64 exec, exec, s[8:9]
	v_add_u32_e32 v4, s54, v224
	v_cmp_lt_i32_e32 vcc, v4, v8
	s_and_saveexec_b64 s[6:7], vcc
	s_cbranch_execz .LBB0_896
	v_ashrrev_i32_e32 v5, 31, v4
	v_lshl_add_u64 v[2:3], v[4:5], 2, v[2:3]
	global_load_dword v5, v[2:3], off
.LBB0_896:
	s_or_b64 exec, exec, s[6:7]
	s_waitcnt vmcnt(0)
	v_lshlrev_b32_e32 v6, 11, v6
	v_lshlrev_b32_e32 v7, 11, v7
	v_lshlrev_b32_e32 v9, 11, v9
	v_lshlrev_b32_e32 v5, 11, v5
	v_or_b32_e32 v235, v9, v225
	v_or_b32_e32 v236, v7, v225
	v_or_b32_e32 v237, v6, v225
	v_or_b32_e32 v238, v5, v225

; #define PG8_STAGE_A(bufoff, gbase, h, VG) do { if constexpr (Sched::GATHER) { PG8_STAGE(bufoff, gbase, VG[h]); } else { PG8_STAGE(bufoff, (gbase) + (h) * ahs, voffA); } } while (0)
; #define PG8_STAGE_B(bufoff, gbase, h) PG8_STAGE(bufoff, (gbase) + (h) * bhs, voffB)
; #define PG8_WAIT_V(n) asm volatile("s_waitcnt vmcnt(" #n ")" ::: "memory")
; #define PG8_BAR __builtin_amdgcn_s_barrier()
;     DI unsigned rowoff(const pg8::GU& u, int r) const { const int gr = 256 * u.pm + r; const int tok = gr < MT[128 + u.e] ? LIST[(size_t)u.e * MOE_CAP + gr] : NTOK; return (unsigned)tok * (unsigned)lda; }
;     DI bool next(int i, pg8::GU& u) const { int pm, pn; if (!T.tile(i, pm, pn)) return false; u.pm = pm; u.pn = pn; u.e = 0; u.aux = 0; u.h1 = 0; u.a = A + (size_t)pm * 256 * lda; u.b = Bt + (size_t)pn * 256 * ldb; return true; }
; template <class Epi, class Sched>
; DI void gemm_phase(LAS unsigned char* lds, const Sched& S, const Epi& E) {
;     ...
;     if constexpr (Sched::GATHER) {
; #pragma unroll
;         for (int h = 0; h < 2; ++h)
; #pragma unroll
;             for (int i = 0; i < 2; ++i) { vc[h][i] = S.rowoff(cur, RR[i] + 128 * h) + (unsigned)(CC[i] * 2); vn[h][i] = vc[h][i]; }
;     } else {
; #pragma unroll
;         for (int h = 0; h < 2; ++h)
; #pragma unroll
;             for (int i = 0; i < 2; ++i) { vc[h][i] = 0u; vn[h][i] = 0u; }
;     }
;     const char* cA = cur.a; const char* cB = cur.b;
;     if constexpr (PG8_SP2) {
;         PG8_STAGE_B(PG8_SB(0, 0), cB, 0); PG8_STAGE_B(PG8_SB(0, 1), cB, 1); PG8_STAGE_A(PG8_SA(0, 0), cA, 0, vc); PG8_STAGE_A(PG8_SA(0, 1), cA, 1, vc);
;         if (wr == 1) PG8_BAR;
;         PG8_WAIT_V(2); PG8_BAR;
;         PG8_STAGE_B(PG8_SB(1, 0), cB + kstep, 0); PG8_STAGE_A(PG8_SA(1, 0), cA + kstep, 0, vc); PG8_STAGE_B(PG8_SB(1, 1), cB + kstep, 1);
;         PG8_WAIT_V(6); PG8_BAR;
;     DI bool next(int i, pg8::GU& u) const {
;         const int L = i * G + c, T = MT[64 + 32]; if (L >= T * 4) return false;
;         const int rt = L >> 2, ct = L & 3; const int e = MT[192 + rt];
;         const int lt = rt - MT[64 + e];
;         u.e = e; u.pm = lt; u.pn = ct; u.aux = MT[e] + 256 * lt; u.h1 = (MT[128 + e] - 256 * lt) <= 128; u.a = Hb; u.b = EG + (size_t)e * estride + (size_t)ct * 128 * ldb; return true;
;     }
.LBB0_1605:
	s_or_b64 exec, exec, s[2:3]
	s_waitcnt vmcnt(0)
	v_lshlrev_b32_e32 v7, 11, v7
	v_lshlrev_b32_e32 v8, 11, v8
	v_lshlrev_b32_e32 v11, 11, v11
	v_lshlrev_b32_e32 v5, 11, v5
	v_and_b32_e32 v2, 32, v0
	v_bitop3_b32 v2, v13, v2, 48 bitop3:0x6c
	v_and_or_b32 v225, v0, 64, v2
	s_lshr_b32 s3, s8, 6
	v_lshlrev_b32_e32 v2, 1, v12
	v_lshrrev_b32_e32 v3, 5, v0
	s_lshl_b32 s6, s3, 10
	v_and_b32_e32 v2, 24, v2
	v_and_b32_e32 v3, 4, v3
	v_and_b32_e32 v4, 3, v12
	v_or3_b32 v2, v3, v4, v2
	s_add_i32 s54, s6, 0
	s_lshr_b32 s2, s8, 8
	v_or_b32_e32 v3, v2, v198
	s_movk_i32 s7, 0x60
	s_add_i32 s55, s54, 0x10000
	s_add_i32 s56, s54, 0x12000
	v_lshl_or_b32 v202, v3, 11, v225
	v_and_or_b32 v2, v6, s7, v2
	s_mov_b32 m0, s55
	s_add_u32 s6, s4, 0x8000000
	v_lshl_or_b32 v204, v2, 11, v225
	global_load_lds_dwordx4 v202, s[4:5]
	s_mov_b32 m0, s56
	s_addc_u32 s7, s5, 0
	s_add_i32 s57, s54, 0x14000
	global_load_lds_dwordx4 v204, s[4:5]
	s_mov_b32 m0, s57
	s_add_i32 s58, s54, 0x16000
	global_load_lds_dwordx4 v202, s[6:7]
	s_mov_b32 m0, s58
	v_or_b32_e32 v210, v7, v225
	global_load_lds_dwordx4 v204, s[6:7]
	s_mov_b32 m0, s54
	s_add_i32 s59, s54, 0x2000
	v_or_b32_e32 v208, v8, v225
	global_load_lds_dwordx4 v210, s[34:35]
	s_mov_b32 m0, s59
	s_add_i32 s60, s54, 0x4000
	v_or_b32_e32 v206, v11, v225
	global_load_lds_dwordx4 v208, s[34:35]
	s_mov_b32 m0, s60
	s_add_i32 s61, s54, 0x6000
	v_or_b32_e32 v212, v5, v225
	global_load_lds_dwordx4 v206, s[34:35]
	s_mov_b32 m0, s61
	v_mov_b32_e32 v67, 0
	global_load_lds_dwordx4 v212, s[34:35]
	v_mov_b32_e32 v203, v67
	v_mov_b32_e32 v205, v67
	v_mov_b32_e32 v211, v67
	v_mov_b32_e32 v209, v67
	s_cmp_eq_u32 s2, 1
	s_mov_b32 s62, 0
	s_mov_b32 s63, 0x10000
	v_lshl_add_u64 v[8:9], s[4:5], 0, v[202:203]
	v_lshl_add_u64 v[4:5], s[4:5], 0, v[204:205]
	s_mov_b32 s66, 0x12000
	s_mov_b32 s67, 0x14000
	v_lshl_add_u64 v[6:7], s[34:35], 0, v[210:211]
	v_lshl_add_u64 v[2:3], s[34:35], 0, v[208:209]
	s_movk_i32 s68, 0x2000
	s_cselect_b64 s[12:13], -1, 0
	s_cmp_lg_u32 s2, 1
	s_movk_i32 s69, 0x4000
	s_cbranch_scc1 .LBB0_1607
	s_barrier

;     DI unsigned rowoff(const pg8::GU& u, int r) const { const int gr = 256 * u.pm + r; const int tok = gr < MT[128 + u.e] ? LIST[(size_t)u.e * MOE_CAP + gr] : NTOK; return (unsigned)tok * (unsigned)lda; }
;     DI bool next(int i, pg8::GU& u) const { int pm, pn; if (!T.tile(i, pm, pn)) return false; u.pm = pm; u.pn = pn; u.e = 0; u.aux = 0; u.h1 = 0; u.a = A + (size_t)pm * 256 * lda; u.b = Bt + (size_t)pn * 256 * ldb; return true; }
; template <class Epi, class Sched>
; DI void gemm_phase(LAS unsigned char* lds, const Sched& S, const Epi& E) {
;     ...
;         if constexpr (Sched::GATHER) {
;             if (has_next) {
; #pragma unroll
;                 for (int h = 0; h < 2; ++h)
; #pragma unroll
;                     for (int i = 0; i < 2; ++i) vn[h][i] = S.rowoff(nxt, RR[i] + 128 * h) + (unsigned)(CC[i] * 2);
;     DI bool next(int i, pg8::GU& u) const {
;         const int L = i * G + c, T = MT[64 + 32]; if (L >= T * 4) return false;
;         const int rt = L >> 2, ct = L & 3; const int e = MT[192 + rt];
;         const int lt = rt - MT[64 + e];
;         u.e = e; u.pm = lt; u.pn = ct; u.aux = MT[e] + 256 * lt; u.h1 = (MT[128 + e] - 256 * lt) <= 128; u.a = Hb; u.b = EG + (size_t)e * estride + (size_t)ct * 128 * ldb; return true;
;     }
.LBB0_1612:
	v_cndmask_b32_e64 v2, 0, 1, s[6:7]
	v_cmp_ne_u32_e64 s[2:3], 1, v2
	s_andn2_b64 vcc, exec, s[6:7]
	v_mov_b32_e32 v238, v212
	v_mov_b32_e32 v235, v206
	v_mov_b32_e32 v236, v208
	v_mov_b32_e32 v237, v210
	s_cbranch_vccnz .LBB0_1622
	v_lshlrev_b32_e32 v2, 2, v232
	v_add_u32_e32 v2, 0, v2
	v_add_u32_e32 v2, 0x22240, v2
	ds_read_b32 v8, v2
	s_lshl_b32 s6, s83, 8
	v_mul_hi_i32 v3, v232, s78
	v_mul_lo_u32 v2, v232, s78
	v_or_b32_e32 v4, s6, v200
	v_lshl_add_u64 v[2:3], s[10:11], 0, v[2:3]
	s_waitcnt lgkmcnt(0)
	v_cmp_lt_i32_e32 vcc, v4, v8
	v_mov_b32_e32 v7, 0x2400
	v_mov_b32_e32 v6, 0x2400
	s_and_saveexec_b64 s[8:9], vcc
	s_cbranch_execz .LBB0_1615
	v_ashrrev_i32_e32 v5, 31, v4
	v_lshl_add_u64 v[4:5], v[4:5], 2, v[2:3]
	global_load_dword v6, v[4:5], off

;     DI unsigned rowoff(const pg8::GU& u, int r) const { const int gr = 256 * u.pm + r; const int tok = gr < MT[128 + u.e] ? LIST[(size_t)u.e * MOE_CAP + gr] : NTOK; return (unsigned)tok * (unsigned)lda; }
;     DI bool next(int i, pg8::GU& u) const { int pm, pn; if (!T.tile(i, pm, pn)) return false; u.pm = pm; u.pn = pn; u.e = 0; u.aux = 0; u.h1 = 0; u.a = A + (size_t)pm * 256 * lda; u.b = Bt + (size_t)pn * 256 * ldb; return true; }
; template <class Epi, class Sched>
; DI void gemm_phase(LAS unsigned char* lds, const Sched& S, const Epi& E) {
;     ...
;         if constexpr (Sched::GATHER) {
;             if (has_next) {
; #pragma unroll
;                 for (int h = 0; h < 2; ++h)
; #pragma unroll
;                     for (int i = 0; i < 2; ++i) vn[h][i] = S.rowoff(nxt, RR[i] + 128 * h) + (unsigned)(CC[i] * 2);
;     DI bool next(int i, pg8::GU& u) const {
;         const int L = i * G + c, T = MT[64 + 32]; if (L >= T * 4) return false;
;         const int rt = L >> 2, ct = L & 3; const int e = MT[192 + rt];
;         const int lt = rt - MT[64 + e];
;         u.e = e; u.pm = lt; u.pn = ct; u.aux = MT[e] + 256 * lt; u.h1 = (MT[128 + e] - 256 * lt) <= 128; u.a = Hb; u.b = EG + (size_t)e * estride + (size_t)ct * 128 * ldb; return true;
;     }
.LBB0_1617:
	s_or_b64 exec, exec, s[8:9]
	s_or_b32 s36, s6, 0x80
	v_or_b32_e32 v4, s36, v200
	v_cmp_lt_i32_e32 vcc, v4, v8
	v_mov_b32_e32 v5, 0x2400
	v_mov_b32_e32 v9, 0x2400
	s_and_saveexec_b64 s[8:9], vcc
	s_cbranch_execz .LBB0_1619
	s_ashr_i32 s7, s6, 31
	v_lshl_add_u64 v[12:13], s[6:7], 0, v[200:201]
	v_lshl_add_u64 v[12:13], v[12:13], 2, v[2:3]
	global_load_dword v9, v[12:13], off offset:512
.LBB0_1619:
	s_or_b64 exec, exec, s[8:9]
	v_add_u32_e32 v4, s36, v224
	v_cmp_lt_i32_e32 vcc, v4, v8
	s_and_saveexec_b64 s[6:7], vcc
	s_cbranch_execz .LBB0_1621
	v_ashrrev_i32_e32 v5, 31, v4
	v_lshl_add_u64 v[2:3], v[4:5], 2, v[2:3]
	global_load_dword v5, v[2:3], off
